# speedup vs baseline: 1.0039x; 1.0039x over previous
.LBB3_20:
	s_and_b64 vcc, exec, s[4:5]
	s_cbranch_vccz .LBB3_26
	s_load_dwordx4 s[8:11], s[0:1], 0x20
	s_load_dwordx2 s[4:5], s[0:1], 0x30
	s_add_i32 s6, s2, 0xffffff00
	s_lshl_b32 s7, s6, 2
	v_lshlrev_b32_e32 v1, 2, v0
	v_add_u32_e32 v2, 0x1000, v1
	s_waitcnt lgkmcnt(0)
	s_add_u32 s10, s10, s7
	s_addc_u32 s11, s11, 0
	s_load_dword s3, s[10:11], 0x0
	s_mul_i32 s7, s6, 0x14000
	s_add_u32 s12, s8, s7
	s_addc_u32 s13, s9, 0
	global_load_dword v16, v1, s[12:13]
	global_load_dword v32, v1, s[12:13] offset:2048
	s_add_u32 s12, s12, 0x1400
	s_addc_u32 s13, s13, 0
	global_load_dword v17, v1, s[12:13]
	global_load_dword v33, v1, s[12:13] offset:2048
	s_add_u32 s12, s12, 0x1400
	s_addc_u32 s13, s13, 0
	global_load_dword v18, v1, s[12:13]
	global_load_dword v34, v1, s[12:13] offset:2048
	s_add_u32 s12, s12, 0x1400
	s_addc_u32 s13, s13, 0
	global_load_dword v19, v1, s[12:13]
	global_load_dword v35, v1, s[12:13] offset:2048
	s_add_u32 s12, s12, 0x1400
	s_addc_u32 s13, s13, 0
	global_load_dword v20, v1, s[12:13]
	global_load_dword v36, v1, s[12:13] offset:2048
	s_add_u32 s12, s12, 0x1400
	s_addc_u32 s13, s13, 0
	global_load_dword v21, v1, s[12:13]
	global_load_dword v37, v1, s[12:13] offset:2048
	s_add_u32 s12, s12, 0x1400
	s_addc_u32 s13, s13, 0
	global_load_dword v22, v1, s[12:13]
	global_load_dword v38, v1, s[12:13] offset:2048
	s_add_u32 s12, s12, 0x1400
	s_addc_u32 s13, s13, 0
	global_load_dword v23, v1, s[12:13]
	global_load_dword v39, v1, s[12:13] offset:2048
	s_add_u32 s12, s12, 0x1400
	s_addc_u32 s13, s13, 0
	global_load_dword v24, v1, s[12:13]
	global_load_dword v40, v1, s[12:13] offset:2048
	s_add_u32 s12, s12, 0x1400
	s_addc_u32 s13, s13, 0
	global_load_dword v25, v1, s[12:13]
	global_load_dword v41, v1, s[12:13] offset:2048
	s_add_u32 s12, s12, 0x1400
	s_addc_u32 s13, s13, 0
	global_load_dword v26, v1, s[12:13]
	global_load_dword v42, v1, s[12:13] offset:2048
	s_add_u32 s12, s12, 0x1400
	s_addc_u32 s13, s13, 0
	global_load_dword v27, v1, s[12:13]
	global_load_dword v43, v1, s[12:13] offset:2048
	s_add_u32 s12, s12, 0x1400
	s_addc_u32 s13, s13, 0
	global_load_dword v28, v1, s[12:13]
	global_load_dword v44, v1, s[12:13] offset:2048
	s_add_u32 s12, s12, 0x1400
	s_addc_u32 s13, s13, 0
	global_load_dword v29, v1, s[12:13]
	global_load_dword v45, v1, s[12:13] offset:2048
	s_add_u32 s12, s12, 0x1400
	s_addc_u32 s13, s13, 0
	global_load_dword v30, v1, s[12:13]
	global_load_dword v46, v1, s[12:13] offset:2048
	s_add_u32 s12, s12, 0x1400
	s_addc_u32 s13, s13, 0
	global_load_dword v31, v1, s[12:13]
	global_load_dword v47, v1, s[12:13] offset:2048
	v_cmp_gt_u32_e32 vcc, 0x100, v0
	s_and_saveexec_b64 s[14:15], vcc
	s_cbranch_execz .Lmy_ca_nok2
	s_add_u32 s12, s8, s7
	s_addc_u32 s13, s9, 0
	global_load_dword v48, v2, s[12:13]
	s_add_u32 s12, s12, 0x1400
	s_addc_u32 s13, s13, 0
	global_load_dword v49, v2, s[12:13]
	s_add_u32 s12, s12, 0x1400
	s_addc_u32 s13, s13, 0
	global_load_dword v50, v2, s[12:13]
	s_add_u32 s12, s12, 0x1400
	s_addc_u32 s13, s13, 0
	global_load_dword v51, v2, s[12:13]
	s_add_u32 s12, s12, 0x1400
	s_addc_u32 s13, s13, 0
	global_load_dword v52, v2, s[12:13]
	s_add_u32 s12, s12, 0x1400
	s_addc_u32 s13, s13, 0
	global_load_dword v53, v2, s[12:13]
	s_add_u32 s12, s12, 0x1400
	s_addc_u32 s13, s13, 0
	global_load_dword v54, v2, s[12:13]
	s_add_u32 s12, s12, 0x1400
	s_addc_u32 s13, s13, 0
	global_load_dword v55, v2, s[12:13]
	s_add_u32 s12, s12, 0x1400
	s_addc_u32 s13, s13, 0
	global_load_dword v56, v2, s[12:13]
	s_add_u32 s12, s12, 0x1400
	s_addc_u32 s13, s13, 0
	global_load_dword v57, v2, s[12:13]
	s_add_u32 s12, s12, 0x1400
	s_addc_u32 s13, s13, 0
	global_load_dword v58, v2, s[12:13]
	s_add_u32 s12, s12, 0x1400
	s_addc_u32 s13, s13, 0
	global_load_dword v59, v2, s[12:13]
	s_add_u32 s12, s12, 0x1400
	s_addc_u32 s13, s13, 0
	global_load_dword v60, v2, s[12:13]
	s_add_u32 s12, s12, 0x1400
	s_addc_u32 s13, s13, 0
	global_load_dword v61, v2, s[12:13]
	s_add_u32 s12, s12, 0x1400
	s_addc_u32 s13, s13, 0
	global_load_dword v62, v2, s[12:13]
	s_add_u32 s12, s12, 0x1400
	s_addc_u32 s13, s13, 0
	global_load_dword v63, v2, s[12:13]
.Lmy_ca_nok2:
	s_or_b64 exec, exec, s[14:15]
	v_mov_b32_e32 v3, 0x3e21e89b
	s_waitcnt vmcnt(0) lgkmcnt(0)
	v_mul_f32_e32 v6, s3, v3
	v_add_f32_e32 v7, 0, v16
	v_add_f32_e32 v8, 0, v32
	v_add_f32_e32 v7, v7, v17
	v_add_f32_e32 v8, v8, v33
	v_add_f32_e32 v7, v7, v18
	v_add_f32_e32 v8, v8, v34
	v_add_f32_e32 v7, v7, v19
	v_add_f32_e32 v8, v8, v35
	v_add_f32_e32 v7, v7, v20
	v_add_f32_e32 v8, v8, v36
	v_add_f32_e32 v7, v7, v21
	v_add_f32_e32 v8, v8, v37
	v_add_f32_e32 v7, v7, v22
	v_add_f32_e32 v8, v8, v38
	v_add_f32_e32 v7, v7, v23
	v_add_f32_e32 v8, v8, v39
	v_add_f32_e32 v7, v7, v24
	v_add_f32_e32 v8, v8, v40
	v_add_f32_e32 v7, v7, v25
	v_add_f32_e32 v8, v8, v41
	v_add_f32_e32 v7, v7, v26
	v_add_f32_e32 v8, v8, v42
	v_add_f32_e32 v7, v7, v27
	v_add_f32_e32 v8, v8, v43
	v_add_f32_e32 v7, v7, v28
	v_add_f32_e32 v8, v8, v44
	v_add_f32_e32 v7, v7, v29
	v_add_f32_e32 v8, v8, v45
	v_add_f32_e32 v7, v7, v30
	v_add_f32_e32 v8, v8, v46
	v_add_f32_e32 v7, v7, v31
	v_add_f32_e32 v8, v8, v47
	v_mul_f32_e32 v7, v7, v6
	v_mul_f32_e32 v8, v8, v6
	ds_write_b32 v1, v7
	ds_write_b32 v1, v8 offset:2048
	s_and_saveexec_b64 s[14:15], vcc
	s_cbranch_execz .Lmy_ca_nok2b
	v_add_f32_e32 v9, 0, v48
	v_add_f32_e32 v9, v9, v49
	v_add_f32_e32 v9, v9, v50
	v_add_f32_e32 v9, v9, v51
	v_add_f32_e32 v9, v9, v52
	v_add_f32_e32 v9, v9, v53
	v_add_f32_e32 v9, v9, v54
	v_add_f32_e32 v9, v9, v55
	v_add_f32_e32 v9, v9, v56
	v_add_f32_e32 v9, v9, v57
	v_add_f32_e32 v9, v9, v58
	v_add_f32_e32 v9, v9, v59
	v_add_f32_e32 v9, v9, v60
	v_add_f32_e32 v9, v9, v61
	v_add_f32_e32 v9, v9, v62
	v_add_f32_e32 v9, v9, v63
	v_mul_f32_e32 v9, v9, v6
	ds_write_b32 v2, v9
.Lmy_ca_nok2b:
	s_or_b64 exec, exec, s[14:15]
	s_waitcnt lgkmcnt(0)
	s_barrier
	s_and_saveexec_b64 s[8:9], vcc
	s_cbranch_execz .LBB3_25
	v_mul_u32_u24_e32 v1, 20, v0
	s_mul_i32 s3, s6, 0x1400
	ds_read_b32 v10, v1
	ds_read_b32 v11, v1 offset:4
	ds_read_b32 v12, v1 offset:8
	ds_read_b32 v13, v1 offset:12
	ds_read_b32 v14, v1 offset:16
	v_add_u32_e32 v20, s3, v1
	s_waitcnt lgkmcnt(0)
	v_max3_f32 v2, v10, v11, v12
	v_max3_f32 v2, v2, v13, v14
	s_nop 1
	v_mov_b32_dpp v3, v2 quad_perm:[1,0,3,2] row_mask:0xf bank_mask:0xf
	v_max_f32_e32 v2, v2, v3
	s_nop 1
	v_mov_b32_dpp v3, v2 quad_perm:[2,3,0,1] row_mask:0xf bank_mask:0xf
	v_max_f32_e32 v2, v2, v3
	s_nop 1
	v_mov_b32_dpp v3, v2 row_half_mirror row_mask:0xf bank_mask:0xf
	v_max_f32_e32 v2, v2, v3
	v_sub_f32_e32 v10, v10, v2
	v_sub_f32_e32 v11, v11, v2
	v_sub_f32_e32 v12, v12, v2
	v_sub_f32_e32 v13, v13, v2
	v_sub_f32_e32 v14, v14, v2
	v_mul_f32_e32 v10, 0x3fb8aa3b, v10
	v_mul_f32_e32 v11, 0x3fb8aa3b, v11
	v_mul_f32_e32 v12, 0x3fb8aa3b, v12
	v_mul_f32_e32 v13, 0x3fb8aa3b, v13
	v_mul_f32_e32 v14, 0x3fb8aa3b, v14
	v_exp_f32_e32 v10, v10
	v_exp_f32_e32 v11, v11
	v_exp_f32_e32 v12, v12
	v_exp_f32_e32 v13, v13
	v_exp_f32_e32 v14, v14
	v_add_f32_e32 v4, v10, v11
	v_add_f32_e32 v4, v4, v12
	v_add_f32_e32 v4, v4, v13
	s_nop 0
	v_add_f32_e32 v4, v4, v14
	s_nop 1
	v_mov_b32_dpp v3, v4 quad_perm:[1,0,3,2] row_mask:0xf bank_mask:0xf
	v_add_f32_e32 v4, v4, v3
	s_nop 1
	v_mov_b32_dpp v3, v4 quad_perm:[2,3,0,1] row_mask:0xf bank_mask:0xf
	v_add_f32_e32 v4, v4, v3
	s_nop 1
	v_mov_b32_dpp v3, v4 row_half_mirror row_mask:0xf bank_mask:0xf
	v_add_f32_e32 v4, v4, v3
	v_div_scale_f32 v5, s[10:11], v4, v4, 1.0
	v_rcp_f32_e32 v7, v5
	s_nop 0
	v_fma_f32 v9, -v5, v7, 1.0
	v_fmac_f32_e32 v7, v9, v7
	v_div_scale_f32 v9, vcc, 1.0, v4, 1.0
	v_mul_f32_e32 v15, v9, v7
	v_fma_f32 v16, -v5, v15, v9
	v_fmac_f32_e32 v15, v16, v7
	v_fma_f32 v5, -v5, v15, v9
	v_div_fmas_f32 v5, v5, v7, v15
	v_div_fixup_f32 v6, v5, v4, 1.0
	v_mul_f32_e32 v10, v6, v10
	v_mul_f32_e32 v11, v6, v11
	v_mul_f32_e32 v12, v6, v12
	v_mul_f32_e32 v13, v6, v13
	v_mul_f32_e32 v14, v6, v14
	global_store_dword v20, v10, s[4:5]
	global_store_dword v20, v11, s[4:5] offset:4
	global_store_dword v20, v12, s[4:5] offset:8
	global_store_dword v20, v13, s[4:5] offset:12
	global_store_dword v20, v14, s[4:5] offset:16
